# stagger sleep removed, static priority for waves 4-7 in the indexer pass kept (on top of v68)
# baseline (speedup 1.0000x reference)
.LBB0_706:
	s_or_b64 exec, exec, s[0:1]
	s_lshl_b32 s2, s16, 2
	s_andn2_b32 s2, s2, 31
	s_and_b32 s0, s16, 7
	s_and_b32 s1, s13, 1
	s_xor_b32 s6, s2, 0x3e0
	s_cmp_eq_u32 s1, 0
	s_cselect_b32 s1, s2, s6
	s_sub_i32 s6, 0x1fe0, s1
	s_lshl_b32 s25, s0, 13
	s_add_i32 s8, s6, s25
	s_lshl_b32 s2, s0, 20
	s_ashr_i32 s9, s8, 31
	s_ashr_i32 s7, s6, 5
	v_readlane_b32 s0, v254, 49
	s_add_u32 s0, s0, s2
	v_readlane_b32 s1, v254, 50
	s_addc_u32 s1, s1, 0
	s_lshl_b64 s[10:11], s[8:9], 5
	v_lshl_add_u64 v[2:3], v[146:147], 0, s[10:11]
	global_load_dwordx4 v[66:69], v[2:3], off
	global_load_dwordx4 v[70:73], v[2:3], off offset:16
	s_lshl_b64 s[8:9], s[8:9], 10
	v_lshl_add_u64 v[62:63], v[144:145], 0, s[8:9]
	global_load_dwordx4 v[2:5], v[62:63], off
	global_load_dwordx4 v[6:9], v[62:63], off offset:128
	global_load_dwordx4 v[10:13], v[62:63], off offset:256
	global_load_dwordx4 v[14:17], v[62:63], off offset:384
	global_load_dwordx4 v[18:21], v[62:63], off offset:512
	global_load_dwordx4 v[22:25], v[62:63], off offset:640
	global_load_dwordx4 v[26:29], v[62:63], off offset:768
	global_load_dwordx4 v[30:33], v[62:63], off offset:896
	global_load_dwordx4 v[34:37], v[62:63], off offset:64
	global_load_dwordx4 v[38:41], v[62:63], off offset:192
	global_load_dwordx4 v[42:45], v[62:63], off offset:320
	global_load_dwordx4 v[46:49], v[62:63], off offset:448
	global_load_dwordx4 v[50:53], v[62:63], off offset:576
	global_load_dwordx4 v[54:57], v[62:63], off offset:704
	global_load_dwordx4 v[58:61], v[62:63], off offset:832
	s_nop 0
	global_load_dwordx4 v[62:65], v[62:63], off offset:960
	v_lshl_add_u64 v[184:185], s[0:1], 0, v[152:153]
	v_lshl_add_u64 v[184:185], v[184:185], 0, v[154:155]
	s_mov_b64 s[10:11], 0x800
	v_lshl_add_u64 v[186:187], v[184:185], 0, s[10:11]
	global_load_dwordx4 v[134:137], v[184:185], off
	global_load_dwordx4 v[130:133], v[184:185], off offset:1024
	s_mov_b64 s[10:11], 0x1000
	v_lshl_add_u64 v[188:189], v[184:185], 0, s[10:11]
	global_load_dwordx4 v[126:129], v[186:187], off
	global_load_dwordx4 v[122:125], v[186:187], off offset:1024
	s_mov_b64 s[10:11], 0x1800
	v_lshl_add_u64 v[184:185], v[184:185], 0, s[10:11]
	global_load_dwordx4 v[110:113], v[188:189], off
	global_load_dwordx4 v[106:109], v[188:189], off offset:1024
	global_load_dwordx4 v[94:97], v[184:185], off
	global_load_dwordx4 v[90:93], v[184:185], off offset:1024
	s_add_i32 s7, s7, 1
	s_ashr_i32 s9, s6, 4
	s_lshl_b32 s8, s7, 1
	v_lshl_add_u64 v[172:173], s[0:1], 0, v[154:155]
	s_waitcnt lgkmcnt(0)
	s_barrier
	s_waitcnt vmcnt(23)
	v_and_b32_e32 v83, 0xffff0000, v3
	v_lshlrev_b32_e32 v82, 16, v3
	s_waitcnt vmcnt(22)
	v_and_b32_e32 v85, 0xffff0000, v7
	v_mul_f32_e32 v156, 0.5, v66
	v_mul_f32_e32 v158, 0.5, v67
	v_and_b32_e32 v67, 0xffff0000, v2
	v_lshlrev_b32_e32 v66, 16, v2
	v_mul_f32_e32 v160, 0.5, v68
	v_mul_f32_e32 v162, 0.5, v69
	v_and_b32_e32 v69, 0xffff0000, v6
	v_lshlrev_b32_e32 v68, 16, v6
	v_lshlrev_b32_e32 v84, 16, v7
	v_pk_fma_f32 v[66:67], v[156:157], v[66:67], 0 op_sel_hi:[0,1,0]
	v_pk_fma_f32 v[82:83], v[156:157], v[82:83], 0 op_sel_hi:[0,1,0]
	v_mul_f32_e32 v164, 0.5, v70
	v_mul_f32_e32 v166, 0.5, v71
	s_waitcnt vmcnt(21)
	v_and_b32_e32 v71, 0xffff0000, v10
	v_lshlrev_b32_e32 v70, 16, v10
	v_and_b32_e32 v87, 0xffff0000, v11
	v_lshlrev_b32_e32 v86, 16, v11
	v_pk_fma_f32 v[66:67], v[158:159], v[68:69], v[66:67] op_sel_hi:[0,1,1]
	v_pk_fma_f32 v[68:69], v[158:159], v[84:85], v[82:83] op_sel_hi:[0,1,1]
	v_mul_f32_e32 v168, 0.5, v72
	v_mul_f32_e32 v170, 0.5, v73
	s_waitcnt vmcnt(20)
	v_and_b32_e32 v73, 0xffff0000, v14
	v_lshlrev_b32_e32 v72, 16, v14
	v_and_b32_e32 v89, 0xffff0000, v15
	v_lshlrev_b32_e32 v88, 16, v15
	v_pk_fma_f32 v[66:67], v[160:161], v[70:71], v[66:67] op_sel_hi:[0,1,1]
	v_pk_fma_f32 v[68:69], v[160:161], v[86:87], v[68:69] op_sel_hi:[0,1,1]
	s_waitcnt vmcnt(19)
	v_and_b32_e32 v75, 0xffff0000, v18
	v_lshlrev_b32_e32 v74, 16, v18
	v_and_b32_e32 v177, 0xffff0000, v19
	v_lshlrev_b32_e32 v176, 16, v19
	v_pk_fma_f32 v[66:67], v[162:163], v[72:73], v[66:67] op_sel_hi:[0,1,1]
	v_pk_fma_f32 v[68:69], v[162:163], v[88:89], v[68:69] op_sel_hi:[0,1,1]
	s_waitcnt vmcnt(18)
	v_and_b32_e32 v77, 0xffff0000, v22
	v_lshlrev_b32_e32 v76, 16, v22
	v_and_b32_e32 v179, 0xffff0000, v23
	v_lshlrev_b32_e32 v178, 16, v23
	v_pk_fma_f32 v[66:67], v[164:165], v[74:75], v[66:67] op_sel_hi:[0,1,1]
	v_pk_fma_f32 v[68:69], v[164:165], v[176:177], v[68:69] op_sel_hi:[0,1,1]
	s_waitcnt vmcnt(17)
	v_and_b32_e32 v79, 0xffff0000, v26
	v_lshlrev_b32_e32 v78, 16, v26
	v_and_b32_e32 v181, 0xffff0000, v27
	v_lshlrev_b32_e32 v180, 16, v27
	v_pk_fma_f32 v[66:67], v[166:167], v[76:77], v[66:67] op_sel_hi:[0,1,1]
	v_pk_fma_f32 v[68:69], v[166:167], v[178:179], v[68:69] op_sel_hi:[0,1,1]
	s_waitcnt vmcnt(16)
	v_and_b32_e32 v81, 0xffff0000, v30
	v_lshlrev_b32_e32 v80, 16, v30
	v_and_b32_e32 v183, 0xffff0000, v31
	v_lshlrev_b32_e32 v182, 16, v31
	v_pk_fma_f32 v[66:67], v[168:169], v[78:79], v[66:67] op_sel_hi:[0,1,1]
	v_pk_fma_f32 v[68:69], v[168:169], v[180:181], v[68:69] op_sel_hi:[0,1,1]
	v_and_b32_e32 v99, 0xffff0000, v4
	v_lshlrev_b32_e32 v98, 16, v4
	v_pk_fma_f32 v[66:67], v[170:171], v[80:81], v[66:67] op_sel_hi:[0,1,1]
	v_pk_fma_f32 v[68:69], v[170:171], v[182:183], v[68:69] op_sel_hi:[0,1,1]
	v_cvt_pk_bf16_f32 v66, v66, v67
	v_cvt_pk_bf16_f32 v67, v68, v69
	v_pk_fma_f32 v[68:69], v[156:157], v[98:99], 0 op_sel_hi:[0,1,0]
	v_and_b32_e32 v71, 0xffff0000, v8
	v_lshlrev_b32_e32 v70, 16, v8
	v_pk_fma_f32 v[68:69], v[158:159], v[70:71], v[68:69] op_sel_hi:[0,1,1]
	v_and_b32_e32 v71, 0xffff0000, v12
	v_lshlrev_b32_e32 v70, 16, v12
	v_pk_fma_f32 v[68:69], v[160:161], v[70:71], v[68:69] op_sel_hi:[0,1,1]
	v_and_b32_e32 v71, 0xffff0000, v16
	v_lshlrev_b32_e32 v70, 16, v16
	v_pk_fma_f32 v[68:69], v[162:163], v[70:71], v[68:69] op_sel_hi:[0,1,1]
	v_and_b32_e32 v71, 0xffff0000, v20
	v_lshlrev_b32_e32 v70, 16, v20
	v_pk_fma_f32 v[68:69], v[164:165], v[70:71], v[68:69] op_sel_hi:[0,1,1]
	v_and_b32_e32 v71, 0xffff0000, v24
	v_lshlrev_b32_e32 v70, 16, v24
	v_pk_fma_f32 v[68:69], v[166:167], v[70:71], v[68:69] op_sel_hi:[0,1,1]
	v_and_b32_e32 v71, 0xffff0000, v28
	v_lshlrev_b32_e32 v70, 16, v28
	v_pk_fma_f32 v[68:69], v[168:169], v[70:71], v[68:69] op_sel_hi:[0,1,1]
	v_and_b32_e32 v71, 0xffff0000, v32
	v_lshlrev_b32_e32 v70, 16, v32
	v_pk_fma_f32 v[68:69], v[170:171], v[70:71], v[68:69] op_sel_hi:[0,1,1]
	v_and_b32_e32 v71, 0xffff0000, v5
	v_lshlrev_b32_e32 v70, 16, v5
	v_pk_fma_f32 v[70:71], v[156:157], v[70:71], 0 op_sel_hi:[0,1,0]
	v_and_b32_e32 v73, 0xffff0000, v9
	v_lshlrev_b32_e32 v72, 16, v9
	v_pk_fma_f32 v[70:71], v[158:159], v[72:73], v[70:71] op_sel_hi:[0,1,1]
	v_and_b32_e32 v73, 0xffff0000, v13
	v_lshlrev_b32_e32 v72, 16, v13
	v_pk_fma_f32 v[70:71], v[160:161], v[72:73], v[70:71] op_sel_hi:[0,1,1]
	v_and_b32_e32 v73, 0xffff0000, v17
	v_lshlrev_b32_e32 v72, 16, v17
	v_pk_fma_f32 v[70:71], v[162:163], v[72:73], v[70:71] op_sel_hi:[0,1,1]
	v_and_b32_e32 v73, 0xffff0000, v21
	v_lshlrev_b32_e32 v72, 16, v21
	v_pk_fma_f32 v[70:71], v[164:165], v[72:73], v[70:71] op_sel_hi:[0,1,1]
	v_and_b32_e32 v73, 0xffff0000, v25
	v_lshlrev_b32_e32 v72, 16, v25
	v_pk_fma_f32 v[70:71], v[166:167], v[72:73], v[70:71] op_sel_hi:[0,1,1]
	v_and_b32_e32 v73, 0xffff0000, v29
	v_lshlrev_b32_e32 v72, 16, v29
	v_pk_fma_f32 v[70:71], v[168:169], v[72:73], v[70:71] op_sel_hi:[0,1,1]
	v_and_b32_e32 v73, 0xffff0000, v33
	v_lshlrev_b32_e32 v72, 16, v33
	v_pk_fma_f32 v[70:71], v[170:171], v[72:73], v[70:71] op_sel_hi:[0,1,1]
	v_cvt_pk_bf16_f32 v68, v68, v69
	v_cvt_pk_bf16_f32 v69, v70, v71
	s_waitcnt vmcnt(15)
	v_and_b32_e32 v71, 0xffff0000, v34
	v_lshlrev_b32_e32 v70, 16, v34
	v_pk_fma_f32 v[70:71], v[156:157], v[70:71], 0 op_sel_hi:[0,1,0]
	s_waitcnt vmcnt(14)
	v_and_b32_e32 v73, 0xffff0000, v38
	v_lshlrev_b32_e32 v72, 16, v38
	v_pk_fma_f32 v[70:71], v[158:159], v[72:73], v[70:71] op_sel_hi:[0,1,1]
	s_waitcnt vmcnt(13)
	v_and_b32_e32 v73, 0xffff0000, v42
	v_lshlrev_b32_e32 v72, 16, v42
	v_pk_fma_f32 v[70:71], v[160:161], v[72:73], v[70:71] op_sel_hi:[0,1,1]
	s_waitcnt vmcnt(12)
	v_and_b32_e32 v73, 0xffff0000, v46
	v_lshlrev_b32_e32 v72, 16, v46
	v_pk_fma_f32 v[70:71], v[162:163], v[72:73], v[70:71] op_sel_hi:[0,1,1]
	s_waitcnt vmcnt(11)
	v_and_b32_e32 v73, 0xffff0000, v50
	v_lshlrev_b32_e32 v72, 16, v50
	v_pk_fma_f32 v[70:71], v[164:165], v[72:73], v[70:71] op_sel_hi:[0,1,1]
	s_waitcnt vmcnt(10)
	v_and_b32_e32 v73, 0xffff0000, v54
	v_lshlrev_b32_e32 v72, 16, v54
	v_pk_fma_f32 v[70:71], v[166:167], v[72:73], v[70:71] op_sel_hi:[0,1,1]
	s_waitcnt vmcnt(9)
	v_and_b32_e32 v73, 0xffff0000, v58
	v_lshlrev_b32_e32 v72, 16, v58
	v_pk_fma_f32 v[70:71], v[168:169], v[72:73], v[70:71] op_sel_hi:[0,1,1]
	s_waitcnt vmcnt(8)
	v_and_b32_e32 v73, 0xffff0000, v62
	v_lshlrev_b32_e32 v72, 16, v62
	v_pk_fma_f32 v[70:71], v[170:171], v[72:73], v[70:71] op_sel_hi:[0,1,1]
	v_and_b32_e32 v73, 0xffff0000, v35
	v_lshlrev_b32_e32 v72, 16, v35
	v_pk_fma_f32 v[72:73], v[156:157], v[72:73], 0 op_sel_hi:[0,1,0]
	v_and_b32_e32 v75, 0xffff0000, v39
	v_lshlrev_b32_e32 v74, 16, v39
	v_pk_fma_f32 v[72:73], v[158:159], v[74:75], v[72:73] op_sel_hi:[0,1,1]
	v_and_b32_e32 v75, 0xffff0000, v43
	v_lshlrev_b32_e32 v74, 16, v43
	v_pk_fma_f32 v[72:73], v[160:161], v[74:75], v[72:73] op_sel_hi:[0,1,1]
	v_and_b32_e32 v75, 0xffff0000, v47
	v_lshlrev_b32_e32 v74, 16, v47
	v_pk_fma_f32 v[72:73], v[162:163], v[74:75], v[72:73] op_sel_hi:[0,1,1]
	v_and_b32_e32 v75, 0xffff0000, v51
	v_lshlrev_b32_e32 v74, 16, v51
	v_pk_fma_f32 v[72:73], v[164:165], v[74:75], v[72:73] op_sel_hi:[0,1,1]
	v_and_b32_e32 v75, 0xffff0000, v55
	v_lshlrev_b32_e32 v74, 16, v55
	v_pk_fma_f32 v[72:73], v[166:167], v[74:75], v[72:73] op_sel_hi:[0,1,1]
	v_and_b32_e32 v75, 0xffff0000, v59
	v_lshlrev_b32_e32 v74, 16, v59
	v_pk_fma_f32 v[72:73], v[168:169], v[74:75], v[72:73] op_sel_hi:[0,1,1]
	v_and_b32_e32 v75, 0xffff0000, v63
	v_lshlrev_b32_e32 v74, 16, v63
	v_pk_fma_f32 v[72:73], v[170:171], v[74:75], v[72:73] op_sel_hi:[0,1,1]
	v_cvt_pk_bf16_f32 v70, v70, v71
	v_cvt_pk_bf16_f32 v71, v72, v73
	v_and_b32_e32 v73, 0xffff0000, v36
	v_lshlrev_b32_e32 v72, 16, v36
	v_pk_fma_f32 v[72:73], v[156:157], v[72:73], 0 op_sel_hi:[0,1,0]
	v_and_b32_e32 v75, 0xffff0000, v40
	v_lshlrev_b32_e32 v74, 16, v40
	v_pk_fma_f32 v[72:73], v[158:159], v[74:75], v[72:73] op_sel_hi:[0,1,1]
	v_and_b32_e32 v75, 0xffff0000, v44
	v_lshlrev_b32_e32 v74, 16, v44
	v_pk_fma_f32 v[72:73], v[160:161], v[74:75], v[72:73] op_sel_hi:[0,1,1]
	v_and_b32_e32 v75, 0xffff0000, v48
	v_lshlrev_b32_e32 v74, 16, v48
	v_pk_fma_f32 v[72:73], v[162:163], v[74:75], v[72:73] op_sel_hi:[0,1,1]
	v_and_b32_e32 v75, 0xffff0000, v52
	v_lshlrev_b32_e32 v74, 16, v52
	v_pk_fma_f32 v[72:73], v[164:165], v[74:75], v[72:73] op_sel_hi:[0,1,1]
	v_and_b32_e32 v75, 0xffff0000, v56
	v_lshlrev_b32_e32 v74, 16, v56
	v_pk_fma_f32 v[72:73], v[166:167], v[74:75], v[72:73] op_sel_hi:[0,1,1]
	v_and_b32_e32 v75, 0xffff0000, v60
	v_lshlrev_b32_e32 v74, 16, v60
	v_pk_fma_f32 v[72:73], v[168:169], v[74:75], v[72:73] op_sel_hi:[0,1,1]
	v_and_b32_e32 v75, 0xffff0000, v64
	v_lshlrev_b32_e32 v74, 16, v64
	v_pk_fma_f32 v[72:73], v[170:171], v[74:75], v[72:73] op_sel_hi:[0,1,1]
	v_and_b32_e32 v75, 0xffff0000, v37
	v_lshlrev_b32_e32 v74, 16, v37
	v_pk_fma_f32 v[74:75], v[156:157], v[74:75], 0 op_sel_hi:[0,1,0]
	v_and_b32_e32 v77, 0xffff0000, v41
	v_lshlrev_b32_e32 v76, 16, v41
	v_pk_fma_f32 v[74:75], v[158:159], v[76:77], v[74:75] op_sel_hi:[0,1,1]
	v_and_b32_e32 v77, 0xffff0000, v45
	v_lshlrev_b32_e32 v76, 16, v45
	v_pk_fma_f32 v[74:75], v[160:161], v[76:77], v[74:75] op_sel_hi:[0,1,1]
	v_and_b32_e32 v77, 0xffff0000, v49
	v_lshlrev_b32_e32 v76, 16, v49
	v_pk_fma_f32 v[74:75], v[162:163], v[76:77], v[74:75] op_sel_hi:[0,1,1]
	v_and_b32_e32 v77, 0xffff0000, v53
	v_lshlrev_b32_e32 v76, 16, v53
	v_pk_fma_f32 v[74:75], v[164:165], v[76:77], v[74:75] op_sel_hi:[0,1,1]
	v_and_b32_e32 v77, 0xffff0000, v57
	v_lshlrev_b32_e32 v76, 16, v57
	v_pk_fma_f32 v[74:75], v[166:167], v[76:77], v[74:75] op_sel_hi:[0,1,1]
	v_and_b32_e32 v77, 0xffff0000, v61
	v_lshlrev_b32_e32 v76, 16, v61
	v_pk_fma_f32 v[74:75], v[168:169], v[76:77], v[74:75] op_sel_hi:[0,1,1]
	v_and_b32_e32 v77, 0xffff0000, v65
	v_lshlrev_b32_e32 v76, 16, v65
	v_pk_fma_f32 v[74:75], v[170:171], v[76:77], v[74:75] op_sel_hi:[0,1,1]
	v_cvt_pk_bf16_f32 v72, v72, v73
	v_cvt_pk_bf16_f32 v73, v74, v75
	v_readlane_b32 s10, v254, 53
	s_waitcnt vmcnt(0)
	s_add_i32 s9, s10, s9
	s_min_i32 s9, s8, s9
	s_cmp_ge_i32 s12, s9
	s_cbranch_scc1 .LBB0_709
	v_readfirstlane_b32 s0, v138
	s_nop 3
	s_cmp_lt_u32 s0, 16
	s_cbranch_scc1 .Lstagger_skip
	s_setprio 1
